# baseline (speedup 1.0000x reference)
_Z16bilateral_kernelPKfS0_Pf:
	s_load_dwordx2 s[4:5], s[0:1], 0x0
	s_load_dwordx2 s[8:9], s[0:1], 0x10
	s_lshr_b32 s19, s2, 8
	s_and_b32 s0, s2, 7
	s_mulk_i32 s0, 0x60
	s_lshr_b32 s1, s2, 3
	s_add_i32 s1, s0, s1
	s_lshr_b32 s0, s1, 6
	s_lshl_b32 s11, s1, 6
	s_nop 0
	s_and_b32 s11, s11, 0x1c0
	s_lshl_b32 s1, s1, 3
	s_nop 0
	s_and_b32 s10, s1, 0x1c0
	s_mov_b32 s1, 0
	s_lshl_b64 s[2:3], s[0:1], 20
	s_mov_b32 s20, 0xc05dfbe6
	s_mov_b32 s21, 0xc05dfbe6
	s_mov_b32 s22, 0xc0a8390e
	s_mov_b32 s23, 0xc0a8390e
	s_mov_b32 s24, 0xc08211a7
	s_mov_b32 s25, 0xc08211a7
	s_mov_b32 s26, 0xc0bb4cc1
	s_mov_b32 s27, 0xc0bb4cc1
	s_mov_b32 s28, 0xc0f487dc
	s_mov_b32 s29, 0xc0f487dc
	s_mov_b32 s30, 0x3e0bd796
	s_mov_b32 s31, 0x3e0bd796
	s_mov_b32 s32, 0x3f45a90c
	s_mov_b32 s33, 0x3f45a90c
	s_mov_b32 s34, 0x3fa5c782
	s_mov_b32 s35, 0x3fa5c782
	v_and_b32_e32 v118, 15, v0
	v_lshrrev_b32_e32 v115, 2, v0
	v_lshl_or_b32 v113, v118, 2, s11
	v_and_or_b32 v117, v115, 60, s10
	v_min_u32_e32 v116, 0x1fa, v113
	v_sub_u32_e64 v115, v113, 2 clamp
	v_add_u32_e64 v116, 4, v116
	v_cmp_eq_u32_e64 s[16:17], 0, v118
	v_cmp_eq_u32_e32 vcc, 15, v118
	s_nop 1
	v_cndmask_b32_e64 v115, v116, v115, s[16:17]
	s_or_b64 vcc, s[16:17], vcc
	v_lshlrev_b32_e32 v115, 2, v115
	v_mov_b32_e32 v116, 0x7ff00000
	s_nop 0
	v_cndmask_b32_e32 v112, v116, v115, vcc
	s_movk_i32 s18, 0x1fc
	v_cmp_eq_u32_e32 vcc, 0, v113
	v_cmp_eq_u32_e64 s[16:17], s18, v113
	v_lshlrev_b32_e64 v113, 2, v113
	s_mov_b32 s6, 0x100000
	s_mov_b32 s7, 0x20000
	s_mov_b32 s14, 0x100000
	s_mov_b32 s15, 0x20000
	v_sub_u32_e64 v115, v117, 2 clamp
	v_lshlrev_b32_e32 v115, 11, v115
	v_add_u32_e32 v128, v115, v112
	v_add_u32_e64 v129, v115, v113
	v_sub_u32_e64 v115, v117, 1 clamp
	v_lshlrev_b32_e32 v115, 11, v115
	v_add_u32_e32 v130, v115, v112
	v_add_u32_e32 v131, v115, v113
	v_lshlrev_b32_e32 v115, 11, v117
	v_add_u32_e32 v132, v115, v112
	v_add_u32_e32 v133, v115, v113
	v_mov_b32_e64 v114, v133
	v_add_u32_e32 v119, 0x1000, v114
	v_lshlrev_b32_e64 v115, 11, v117
	v_add_u32_e32 v115, 0x800, v115
	v_add_u32_e32 v134, v115, v112
	v_add_u32_e32 v135, v115, v113
	v_lshlrev_b32_e64 v115, 11, v117
	v_add_u32_e32 v115, 0x1000, v115
	v_add_u32_e32 v136, v115, v112
	v_add_u32_e32 v137, v115, v113
	v_lshlrev_b32_e64 v115, 11, v117
	v_add_u32_e32 v115, 0x1800, v115
	v_add_u32_e32 v138, v115, v112
	v_add_u32_e32 v139, v115, v113
	v_min_u32_e32 v115, 0x1fb, v117
	v_lshlrev_b32_e64 v115, 11, v115
	v_add_u32_e32 v115, 0x2000, v115
	v_add_u32_e32 v140, v115, v112
	v_add_u32_e32 v141, v115, v113
	v_min_u32_e32 v115, 0x1fa, v117
	v_lshlrev_b32_e64 v115, 11, v115
	v_add_u32_e32 v115, 0x2800, v115
	v_add_u32_e64 v142, v115, v112
	v_add_u32_e32 v143, v115, v113
	s_waitcnt lgkmcnt(0)
	s_add_u32 s4, s4, s2
	s_addc_u32 s5, s5, s3
	s_and_b32 s5, s5, 0xffff
	buffer_load_dwordx2 v[0:1], v128, s[4:7], 0 offen nt
	buffer_load_dwordx2 v[6:7], v128, s[4:7], 0 offen nt
	buffer_load_dwordx4 v[2:5], v129, s[4:7], 0 offen nt
	buffer_load_dwordx2 v[8:9], v130, s[4:7], 0 offen nt
	buffer_load_dwordx2 v[14:15], v130, s[4:7], 0 offen nt
	buffer_load_dwordx4 v[10:13], v131, s[4:7], 0 offen nt
	buffer_load_dwordx2 v[16:17], v132, s[4:7], 0 offen nt
	buffer_load_dwordx2 v[22:23], v132, s[4:7], 0 offen nt
	buffer_load_dwordx4 v[18:21], v133, s[4:7], 0 offen nt
	buffer_load_dwordx2 v[24:25], v134, s[4:7], 0 offen nt
	buffer_load_dwordx2 v[30:31], v134, s[4:7], 0 offen nt
	buffer_load_dwordx4 v[26:29], v135, s[4:7], 0 offen nt
	buffer_load_dwordx2 v[32:33], v136, s[4:7], 0 offen nt
	buffer_load_dwordx2 v[38:39], v136, s[4:7], 0 offen nt
	buffer_load_dwordx4 v[34:37], v137, s[4:7], 0 offen nt
	buffer_load_dwordx2 v[40:41], v138, s[4:7], 0 offen nt
	buffer_load_dwordx2 v[46:47], v138, s[4:7], 0 offen nt
	buffer_load_dwordx4 v[42:45], v139, s[4:7], 0 offen nt
	buffer_load_dwordx2 v[48:49], v140, s[4:7], 0 offen nt
	buffer_load_dwordx2 v[54:55], v140, s[4:7], 0 offen nt
	buffer_load_dwordx4 v[50:53], v141, s[4:7], 0 offen nt
	buffer_load_dwordx2 v[56:57], v142, s[4:7], 0 offen nt
	buffer_load_dwordx2 v[62:63], v142, s[4:7], 0 offen nt
	buffer_load_dwordx4 v[58:61], v143, s[4:7], 0 offen nt
	s_add_u32 s12, s8, s2
	s_addc_u32 s13, s9, s3
	s_and_b32 s13, s13, 0xffff
	s_cmp_eq_u32 s19, 0
	s_cbranch_scc1 .Lmyp0
	s_cmp_eq_u32 s19, 1
	s_cbranch_scc1 .Lmyp1
	s_setprio 0
	s_branch .Lmypd
